# MoeOrder::next 31-step serial LDS scan replaced by one vector LDS read + v_cmp + s_bcnt1 (4 sites), on top of dead kernarg reload removal
# speedup vs baseline: 1.0091x; 1.0091x over previous
.LBB0_1714:
	v_mbcnt_lo_u32_b32 v2, -1, 0
	v_mbcnt_hi_u32_b32 v2, -1, v2
	v_min_u32_e32 v2, 30, v2
	v_lshlrev_b32_e32 v2, 2, v2
	v_add_u32_e32 v2, 0x20000, v2
	ds_read_b32 v2, v2
	s_waitcnt lgkmcnt(0)
	v_cmp_le_i32_e64 s[2:3], v2, s18
	s_and_b32 s2, s2, 0x7fffffff
	s_bcnt1_i32_b32 s20, s2
	s_movk_i32 s1, 0x7c
	s_cmpk_eq_i32 s1, 0x7c
	v_ashrrev_i32_e32 v3, 31, v11
	v_lshrrev_b32_e32 v3, 26, v3
	v_add_u32_e32 v3, v11, v3
	v_ashrrev_i32_e32 v6, 6, v3
	v_bfe_i32 v3, v11, 27, 1
	v_lshlrev_b32_e32 v2, 4, v11
	v_lshrrev_b32_e32 v3, 22, v3
	v_add_u32_e32 v3, v2, v3
	v_and_b32_e32 v3, 0xfffffc00, v3
	v_sub_u32_e32 v3, v2, v3
	v_lshrrev_b32_e32 v4, 4, v3
	v_bitop3_b32 v3, v4, v3, 32 bitop3:0x6c
	v_ashrrev_i32_e32 v5, 31, v3
	v_lshrrev_b32_e32 v5, 26, v5
	v_add_u32_e32 v5, v3, v5
	v_lshlrev_b32_e32 v4, 3, v6
	v_ashrrev_i32_e32 v7, 6, v5
	v_and_b32_e32 v5, 0xc0, v5
	v_and_b32_e32 v4, -16, v4
	v_sub_u32_e32 v3, v3, v5
	s_lshl_b32 s1, s50, 26
	v_readlane_b32 s2, v251, 51
	v_add_u32_e32 v4, v7, v4
	v_lshlrev_b32_e32 v8, 5, v6
	v_ashrrev_i16_sdwa v3, v178, sext(v3) dst_sel:DWORD dst_unused:UNUSED_PAD src0_sel:DWORD src1_sel:BYTE_0
	s_add_u32 s24, s2, s1
	v_and_b32_e32 v9, 32, v8
	v_bfe_i32 v8, v3, 0, 16
	v_lshlrev_b32_e32 v3, 1, v4
	v_lshrrev_b32_e32 v5, 2, v4
	v_and_b32_e32 v10, 3, v7
	s_mov_b32 s2, 0x1fffe0
	v_and_b32_e32 v3, 24, v3
	v_and_b32_e32 v5, 4, v5
	v_and_or_b32 v10, v4, s2, v10
	v_or3_b32 v3, v10, v5, v3
	v_add_lshl_u32 v5, v9, v8, 1
	v_add_u32_e32 v2, 0x2000, v2
	v_lshl_add_u32 v162, v3, 11, v5
	v_ashrrev_i32_e32 v3, 31, v2
	v_lshrrev_b32_e32 v3, 22, v3
	v_add_u32_e32 v3, v2, v3
	v_ashrrev_i32_e32 v9, 10, v3
	v_mul_i32_i24_e32 v3, 0x400, v9
	v_sub_u32_e32 v2, v2, v3
	v_lshrrev_b32_e32 v3, 4, v2
	v_bitop3_b32 v2, v3, v2, 32 bitop3:0x6c
	v_lshl_add_u32 v130, v4, 11, v5
	v_ashrrev_i32_e32 v4, 31, v2
	v_lshrrev_b32_e32 v4, 26, v4
	v_readlane_b32 s1, v251, 52
	v_lshlrev_b32_e32 v3, 3, v9
	v_add_u32_e32 v4, v2, v4
	s_addc_u32 s25, s1, 0
	v_readlane_b32 s1, v253, 54
	v_and_b32_e32 v3, -16, v3
	v_ashrrev_i32_e32 v10, 6, v4
	s_add_u32 s3, s24, s1
	v_add_u32_e32 v3, v10, v3
	v_and_b32_e32 v13, 3, v10
	s_addc_u32 s4, s25, 0
	v_and_b32_e32 v4, 0xc0, v4
	v_and_or_b32 v13, v3, s2, v13
	s_ashr_i32 s2, s0, 6
	s_ashr_i32 s1, s0, 8
	v_sub_u32_e32 v2, v2, v4
	s_lshl_b32 s48, s2, 10
	s_lshl_b64 s[6:7], s[20:21], 21
	v_ashrrev_i16_sdwa v2, v178, sext(v2) dst_sel:DWORD dst_unused:UNUSED_PAD src0_sel:DWORD src1_sel:BYTE_0
	s_add_u32 s8, s3, s6
	v_lshlrev_b32_e32 v5, 5, v9
	v_bfe_i32 v12, v2, 0, 16
	v_lshlrev_b32_e32 v2, 1, v3
	v_lshrrev_b32_e32 v4, 2, v3
	s_addc_u32 s9, s4, s7
	s_add_i32 s49, s48, 0
	v_and_b32_e32 v5, 32, v5
	v_and_b32_e32 v2, 24, v2
	v_and_b32_e32 v4, 4, v4
	s_add_i32 m0, s49, 0x10000
	v_or3_b32 v2, v13, v4, v2
	v_add_lshl_u32 v4, v5, v12, 1
	global_load_lds_dwordx4 v162, s[8:9]
	s_add_i32 m0, s49, 0x12000
	v_lshl_add_u32 v134, v2, 11, v4
	s_add_u32 s6, s8, 0x40000
	global_load_lds_dwordx4 v134, s[8:9]
	s_addc_u32 s7, s9, 0
	s_add_i32 m0, s49, 0x14000
	s_mov_b32 s62, s50
	global_load_lds_dwordx4 v162, s[6:7]
	s_add_i32 m0, s49, 0x16000
	s_add_i32 s50, s49, 0x2000
	global_load_lds_dwordx4 v134, s[6:7]
	v_readlane_b32 s6, v253, 55
	s_mov_b32 m0, s49
	v_readlane_b32 s7, v253, 56
	v_lshl_add_u32 v132, v3, 11, v4
	s_add_i32 s51, s49, 0x4000
	s_add_i32 s52, s49, 0x6000
	s_cmp_eq_u32 s1, 1
	v_mov_b32_e32 v135, v163
	global_load_lds_dwordx4 v130, s[6:7]
	s_mov_b32 m0, s50
	v_lshl_add_u64 v[4:5], s[8:9], 0, v[162:163]
	global_load_lds_dwordx4 v132, s[6:7]
	v_readlane_b32 s6, v253, 57
	s_mov_b32 m0, s51
	v_readlane_b32 s7, v253, 58
	v_lshl_add_u64 v[2:3], s[8:9], 0, v[134:135]
	s_nop 3
	global_load_lds_dwordx4 v130, s[6:7]
	s_mov_b32 m0, s52
	s_nop 0
	global_load_lds_dwordx4 v132, s[6:7]
	s_cselect_b64 s[6:7], -1, 0
	s_and_b64 vcc, exec, s[6:7]
	s_cbranch_vccz .LBB0_1717
	s_barrier

.LBB0_1722:
	v_mbcnt_lo_u32_b32 v2, -1, 0
	v_mbcnt_hi_u32_b32 v2, -1, v2
	v_min_u32_e32 v2, 30, v2
	v_lshlrev_b32_e32 v2, 2, v2
	v_add_u32_e32 v2, 0x20000, v2
	ds_read_b32 v2, v2
	s_waitcnt lgkmcnt(0)
	v_cmp_le_i32_e64 s[38:39], v2, s18
	s_and_b32 s38, s38, 0x7fffffff
	s_bcnt1_i32_b32 s20, s38
	s_movk_i32 s3, 0x7c
	s_cmpk_eq_i32 s3, 0x7c
	s_and_b32 s38, s2, 3
	s_lshl_b64 s[42:43], s[20:21], 21

.LBB0_1791:
	v_mbcnt_lo_u32_b32 v2, -1, 0
	v_mbcnt_hi_u32_b32 v2, -1, v2
	v_min_u32_e32 v2, 30, v2
	v_lshlrev_b32_e32 v2, 2, v2
	v_add_u32_e32 v2, 0x20000, v2
	ds_read_b32 v2, v2
	s_waitcnt lgkmcnt(0)
	v_cmp_le_i32_e64 s[2:3], v2, s4
	s_and_b32 s2, s2, 0x7fffffff
	s_bcnt1_i32_b32 s20, s2
	s_movk_i32 s1, 0x7c
	s_cmpk_eq_i32 s1, 0x7c
	v_ashrrev_i32_e32 v3, 31, v11
	v_lshrrev_b32_e32 v3, 26, v3
	v_add_u32_e32 v3, v11, v3
	v_ashrrev_i32_e32 v6, 6, v3
	v_bfe_i32 v3, v11, 27, 1
	v_lshlrev_b32_e32 v2, 4, v11
	v_lshrrev_b32_e32 v3, 22, v3
	v_add_u32_e32 v3, v2, v3
	v_and_b32_e32 v3, 0xfffffc00, v3
	v_sub_u32_e32 v3, v2, v3
	v_lshrrev_b32_e32 v4, 4, v3
	v_bitop3_b32 v3, v4, v3, 32 bitop3:0x6c
	v_ashrrev_i32_e32 v5, 31, v3
	v_lshrrev_b32_e32 v5, 26, v5
	v_add_u32_e32 v5, v3, v5
	v_lshlrev_b32_e32 v4, 3, v6
	v_ashrrev_i32_e32 v7, 6, v5
	v_and_b32_e32 v5, 0xc0, v5
	v_and_b32_e32 v4, -16, v4
	v_sub_u32_e32 v3, v3, v5
	s_lshl_b32 s1, s50, 25
	v_readlane_b32 s2, v251, 49
	v_add_u32_e32 v4, v7, v4
	v_lshlrev_b32_e32 v8, 5, v6
	v_ashrrev_i16_sdwa v3, v178, sext(v3) dst_sel:DWORD dst_unused:UNUSED_PAD src0_sel:DWORD src1_sel:BYTE_0
	s_add_u32 s10, s2, s1
	v_and_b32_e32 v9, 32, v8
	v_bfe_i32 v8, v3, 0, 16
	v_lshlrev_b32_e32 v3, 1, v4
	v_lshrrev_b32_e32 v5, 2, v4
	v_and_b32_e32 v10, 3, v7
	s_mov_b32 s2, 0x3fffe0
	v_and_b32_e32 v3, 24, v3
	v_and_b32_e32 v5, 4, v5
	v_and_or_b32 v10, v4, s2, v10
	v_or3_b32 v3, v10, v5, v3
	v_add_lshl_u32 v5, v9, v8, 1
	v_add_u32_e32 v2, 0x2000, v2
	v_lshl_add_u32 v162, v3, 10, v5
	v_ashrrev_i32_e32 v3, 31, v2
	v_lshrrev_b32_e32 v3, 22, v3
	v_add_u32_e32 v3, v2, v3
	v_ashrrev_i32_e32 v9, 10, v3
	v_mul_i32_i24_e32 v3, 0x400, v9
	v_sub_u32_e32 v2, v2, v3
	v_lshrrev_b32_e32 v3, 4, v2
	v_bitop3_b32 v2, v3, v2, 32 bitop3:0x6c
	v_lshl_add_u32 v130, v4, 10, v5
	v_ashrrev_i32_e32 v4, 31, v2
	v_lshrrev_b32_e32 v4, 26, v4
	v_readlane_b32 s1, v251, 50
	v_lshlrev_b32_e32 v3, 3, v9
	v_add_u32_e32 v4, v2, v4
	s_addc_u32 s11, s1, 0
	v_readlane_b32 s1, v253, 60
	v_and_b32_e32 v3, -16, v3
	v_ashrrev_i32_e32 v10, 6, v4
	s_add_u32 s3, s10, s1
	v_add_u32_e32 v3, v10, v3
	v_and_b32_e32 v13, 3, v10
	s_addc_u32 s4, s11, 0
	v_and_b32_e32 v4, 0xc0, v4
	v_and_or_b32 v13, v3, s2, v13
	s_ashr_i32 s2, s0, 6
	s_ashr_i32 s1, s0, 8
	v_sub_u32_e32 v2, v2, v4
	s_lshl_b32 s33, s2, 10
	s_lshl_b64 s[6:7], s[20:21], 20
	v_ashrrev_i16_sdwa v2, v178, sext(v2) dst_sel:DWORD dst_unused:UNUSED_PAD src0_sel:DWORD src1_sel:BYTE_0
	s_add_u32 s8, s3, s6
	v_lshlrev_b32_e32 v5, 5, v9
	v_bfe_i32 v12, v2, 0, 16
	v_lshlrev_b32_e32 v2, 1, v3
	v_lshrrev_b32_e32 v4, 2, v3
	s_addc_u32 s9, s4, s7
	s_add_i32 s46, s33, 0
	v_and_b32_e32 v5, 32, v5
	v_and_b32_e32 v2, 24, v2
	v_and_b32_e32 v4, 4, v4
	s_add_i32 m0, s46, 0x10000
	v_or3_b32 v2, v13, v4, v2
	v_add_lshl_u32 v4, v5, v12, 1
	global_load_lds_dwordx4 v162, s[8:9]
	s_add_i32 m0, s46, 0x12000
	v_lshl_add_u32 v134, v2, 10, v4
	s_add_u32 s6, s8, 0x20000
	global_load_lds_dwordx4 v134, s[8:9]
	s_addc_u32 s7, s9, 0
	s_add_i32 m0, s46, 0x14000
	s_add_i32 s47, s46, 0x2000
	global_load_lds_dwordx4 v162, s[6:7]
	s_add_i32 m0, s46, 0x16000
	v_lshl_add_u32 v132, v3, 10, v4
	global_load_lds_dwordx4 v134, s[6:7]
	v_readlane_b32 s6, v253, 63
	s_mov_b32 m0, s46
	v_readlane_b32 s7, v254, 0
	s_add_i32 s48, s46, 0x4000
	s_add_i32 s49, s46, 0x6000
	s_cmp_eq_u32 s1, 1
	v_mov_b32_e32 v135, v163
	s_mov_b32 s62, s50
	global_load_lds_dwordx4 v130, s[6:7]
	s_mov_b32 m0, s47
	v_lshl_add_u64 v[4:5], s[8:9], 0, v[162:163]
	global_load_lds_dwordx4 v132, s[6:7]
	v_readlane_b32 s6, v254, 1
	s_mov_b32 m0, s48
	v_readlane_b32 s7, v254, 2
	v_lshl_add_u64 v[2:3], s[8:9], 0, v[134:135]
	s_nop 3
	global_load_lds_dwordx4 v130, s[6:7]
	s_mov_b32 m0, s49
	s_nop 0
	global_load_lds_dwordx4 v132, s[6:7]
	s_cselect_b64 s[6:7], -1, 0
	s_and_b64 vcc, exec, s[6:7]
	s_cbranch_vccz .LBB0_1794
	s_barrier

.LBB0_1799:
	v_mbcnt_lo_u32_b32 v2, -1, 0
	v_mbcnt_hi_u32_b32 v2, -1, v2
	v_min_u32_e32 v2, 30, v2
	v_lshlrev_b32_e32 v2, 2, v2
	v_add_u32_e32 v2, 0x20000, v2
	ds_read_b32 v2, v2
	s_waitcnt lgkmcnt(0)
	v_cmp_le_i32_e64 s[24:25], v2, s18
	s_and_b32 s24, s24, 0x7fffffff
	s_bcnt1_i32_b32 s20, s24
	s_movk_i32 s3, 0x7c
	s_cmpk_eq_i32 s3, 0x7c
	s_and_b32 s24, s2, 3
	s_lshl_b64 s[38:39], s[20:21], 20
